# hot loop heads of attention and gemm_qkv aligned to 64 bytes
# speedup vs baseline: 1.0315x; 1.0000x over previous
.LBB2_2:
	v_lshrrev_b32_e32 v14, 4, v0
	v_and_b32_e32 v1, 15, v0
	v_bfe_u32 v17, v0, 1, 3
	s_and_b32 s1, s18, 3
	v_lshlrev_b32_e32 v15, 7, v1
	v_bitop3_b32 v14, v14, v17, 3 bitop3:0x6c
	v_bfe_u32 v106, v0, 4, 2
	v_lshl_or_b32 v16, s25, 13, v15
	v_lshl_or_b32 v18, s1, 12, v15
	v_lshl_or_b32 v15, s1, 11, v15
	v_lshlrev_b32_e32 v14, 4, v14
	v_or_b32_e32 v19, v14, v16
	v_or_b32_e32 v20, v14, v18
	v_or_b32_e32 v21, v14, v15
	v_bitop3_b32 v14, v106, v17, 4 bitop3:0x36
	v_lshlrev_b32_e32 v14, 4, v14
	s_mov_b64 s[18:19], 0x80
	v_or_b32_e32 v16, v14, v16
	v_or_b32_e32 v17, v14, v18
	v_or_b32_e32 v18, v14, v15
	s_add_i32 m0, s27, 0x14000
	v_lshl_add_u64 v[14:15], v[4:5], 0, s[18:19]
	s_waitcnt vmcnt(2)
	s_barrier
	global_load_lds_dwordx4 v[14:15], off
	v_lshl_add_u64 v[10:11], v[10:11], 0, s[18:19]
	s_add_i32 m0, s27, 0x16000
	s_add_i32 s31, s27, 0x8000
	global_load_lds_dwordx4 v[10:11], off
	v_lshl_add_u64 v[8:9], v[8:9], 0, s[18:19]
	s_mov_b32 m0, s31
	s_add_i32 s33, s27, 0xa000
	global_load_lds_dwordx4 v[8:9], off
	v_lshl_add_u64 v[6:7], v[6:7], 0, s[18:19]
	s_mov_b32 m0, s33
	s_mov_b64 s[20:21], 0x40080
	global_load_lds_dwordx4 v[6:7], off
	v_lshl_add_u64 v[4:5], v[4:5], 0, s[20:21]
	s_add_i32 m0, s27, 0x1a000
	s_and_b32 s2, s2, 3
	global_load_lds_dwordx4 v[4:5], off
	s_mul_i32 s2, s2, 0xc0000
	s_mul_i32 s3, s3, 0x30000
	s_add_i32 s2, s2, s3
	s_lshl_b32 s2, s2, 1
	s_add_u32 s2, s6, s2
	s_addc_u32 s3, s7, 0
	s_add_u32 s6, s2, 0x100
	s_addc_u32 s7, s3, 0
	s_add_u32 s2, s4, s22
	v_add_u32_e32 v4, v13, v3
	v_mov_b32_e32 v5, v2
	s_addc_u32 s3, s5, s23
	v_lshl_add_u64 v[4:5], s[2:3], 0, v[4:5]
	s_add_i32 s4, 0, 0x10800
	s_waitcnt vmcnt(5)
	v_lshl_add_u64 v[102:103], v[4:5], 0, s[20:21]
	v_add_u32_e32 v4, v12, v3
	v_mov_b32_e32 v5, v2
	s_add_i32 s35, 0, 0x10000
	v_add_u32_e32 v109, s4, v20
	v_add_u32_e32 v110, s4, v17
	s_add_i32 s38, 0, 0x14000
	s_add_i32 s4, 0, 0x14800
	v_lshl_add_u64 v[4:5], s[2:3], 0, v[4:5]
	v_add_u32_e32 v107, s35, v20
	v_add_u32_e32 v108, s35, v17
	s_add_i32 s37, 0, 0x18000
	s_add_i32 s35, s35, s40
	v_add_u32_e32 v115, s38, v20
	v_add_u32_e32 v116, s38, v17
	v_add_u32_e32 v117, s4, v20
	v_add_u32_e32 v118, s4, v17
	s_add_i32 s4, 0, 0x1a000
	s_add_i32 s38, s38, s40
	v_lshl_add_u64 v[104:105], v[4:5], 0, s[20:21]
	s_mov_b32 s22, -2
	s_mov_b64 s[2:3], 0
	v_add_u32_e32 v111, s37, v21
	v_add_u32_e32 v112, s37, v18
	v_add_u32_e32 v113, 0, v19
	v_add_u32_e32 v114, 0, v16
	s_add_i32 s23, s27, 0xc000
	s_add_i32 s34, s27, 0xe000
	s_add_i32 s36, s35, 0x2000
	s_add_i32 s37, s37, s40
	v_add_u32_e32 v119, s4, v21
	v_add_u32_e32 v120, s4, v18
	s_add_i32 s39, s38, 0x2000
	s_add_i32 s40, s4, s40
	v_mov_b32_e32 v3, v2
	v_mov_b32_e32 v4, v2
	v_mov_b32_e32 v5, v2
	v_mov_b32_e32 v62, v2
	v_mov_b32_e32 v63, v2
	v_mov_b32_e32 v64, v2
	v_mov_b32_e32 v65, v2
	v_mov_b32_e32 v22, v2
	v_mov_b32_e32 v23, v2
	v_mov_b32_e32 v24, v2
	v_mov_b32_e32 v25, v2
	v_mov_b32_e32 v66, v2
	v_mov_b32_e32 v67, v2
	v_mov_b32_e32 v68, v2
	v_mov_b32_e32 v69, v2
	v_mov_b32_e32 v30, v2
	v_mov_b32_e32 v31, v2
	v_mov_b32_e32 v32, v2
	v_mov_b32_e32 v33, v2
	v_mov_b32_e32 v70, v2
	v_mov_b32_e32 v71, v2
	v_mov_b32_e32 v72, v2
	v_mov_b32_e32 v73, v2
	v_mov_b32_e32 v38, v2
	v_mov_b32_e32 v39, v2
	v_mov_b32_e32 v40, v2
	v_mov_b32_e32 v41, v2
	v_mov_b32_e32 v74, v2
	v_mov_b32_e32 v75, v2
	v_mov_b32_e32 v76, v2
	v_mov_b32_e32 v77, v2
	v_mov_b32_e32 v46, v2
	v_mov_b32_e32 v47, v2
	v_mov_b32_e32 v48, v2
	v_mov_b32_e32 v49, v2
	v_mov_b32_e32 v78, v2
	v_mov_b32_e32 v79, v2
	v_mov_b32_e32 v80, v2
	v_mov_b32_e32 v81, v2
	v_mov_b32_e32 v50, v2
	v_mov_b32_e32 v51, v2
	v_mov_b32_e32 v52, v2
	v_mov_b32_e32 v53, v2
	v_mov_b32_e32 v82, v2
	v_mov_b32_e32 v83, v2
	v_mov_b32_e32 v84, v2
	v_mov_b32_e32 v85, v2
	v_mov_b32_e32 v58, v2
	v_mov_b32_e32 v59, v2
	v_mov_b32_e32 v60, v2
	v_mov_b32_e32 v61, v2
	v_mov_b32_e32 v90, v2
	v_mov_b32_e32 v91, v2
	v_mov_b32_e32 v92, v2
	v_mov_b32_e32 v93, v2
	v_mov_b32_e32 v86, v2
	v_mov_b32_e32 v87, v2
	v_mov_b32_e32 v88, v2
	v_mov_b32_e32 v89, v2
	v_mov_b32_e32 v94, v2
	v_mov_b32_e32 v95, v2
	v_mov_b32_e32 v96, v2
	v_mov_b32_e32 v97, v2
	v_mov_b32_e32 v6, v2
	v_mov_b32_e32 v7, v2
	v_mov_b32_e32 v8, v2
	v_mov_b32_e32 v9, v2
	v_mov_b32_e32 v10, v2
	v_mov_b32_e32 v11, v2
	v_mov_b32_e32 v12, v2
	v_mov_b32_e32 v13, v2
	v_mov_b32_e32 v14, v2
	v_mov_b32_e32 v15, v2
	v_mov_b32_e32 v16, v2
	v_mov_b32_e32 v17, v2
	v_mov_b32_e32 v18, v2
	v_mov_b32_e32 v19, v2
	v_mov_b32_e32 v20, v2
	v_mov_b32_e32 v21, v2
	v_mov_b32_e32 v26, v2
	v_mov_b32_e32 v27, v2
	v_mov_b32_e32 v28, v2
	v_mov_b32_e32 v29, v2
	v_mov_b32_e32 v34, v2
	v_mov_b32_e32 v35, v2
	v_mov_b32_e32 v36, v2
	v_mov_b32_e32 v37, v2
	v_mov_b32_e32 v42, v2
	v_mov_b32_e32 v43, v2
	v_mov_b32_e32 v44, v2
	v_mov_b32_e32 v45, v2
	v_mov_b32_e32 v54, v2
	v_mov_b32_e32 v55, v2
	v_mov_b32_e32 v56, v2
	v_mov_b32_e32 v57, v2
	s_barrier
	.p2align	6

_ZN3att8attn_fwdEPKDF16_PDF16_:
	s_load_dwordx4 s[4:7], s[0:1], 0x0
	s_lshl_b32 s0, s2, 2
	s_and_b32 s0, s0, 28
	s_lshr_b32 s1, s2, 6
	v_readfirstlane_b32 s10, v0
	s_add_i32 s8, s0, s1
	s_lshl_b32 s0, s2, 5
	s_mov_b32 s9, 0
	s_lshr_b32 s26, s10, 6
	s_and_b32 s27, s0, 0x700
	s_lshl_b64 s[0:1], s[8:9], 11
	s_or_b32 s0, s0, s27
	s_lshl_b32 s28, s26, 5
	s_add_u32 s0, s0, s28
	s_addc_u32 s1, s1, 0
	s_lshl_b64 s[0:1], s[0:1], 7
	s_waitcnt lgkmcnt(0)
	s_add_u32 s12, s4, s0
	s_addc_u32 s13, s5, s1
	s_lshl_b64 s[2:3], s[8:9], 18
	s_add_u32 s1, s4, s2
	s_addc_u32 s15, s5, s3
	s_and_b32 s0, s10, 0x3fffffc0
	s_lshl_b32 s10, s26, 9
	s_mov_b32 s11, s9
	s_lshl_b64 s[10:11], s[10:11], 1
	v_and_b32_e32 v190, 63, v0
	s_add_u32 s14, s1, s10
	s_addc_u32 s15, s15, s11
	v_lshlrev_b32_e32 v184, 4, v190
	v_mov_b32_e32 v185, 0
	v_lshl_add_u64 v[48:49], s[14:15], 0, v[184:185]
	s_mov_b64 s[14:15], 0x800000
	s_lshl_b32 s1, s26, 10
	v_lshl_add_u64 v[180:181], v[48:49], 0, s[14:15]
	s_mov_b64 s[14:15], 0x1000000
	s_cmp_lg_u32 0, -1
	v_lshl_add_u64 v[182:183], v[48:49], 0, s[14:15]
	s_cselect_b32 s14, 0, 0
	v_bfe_u32 v192, v0, 5, 1
	s_add_i32 s30, s1, s14
	s_mov_b32 s1, m0
	s_mov_b32 m0, s30
	s_nop 0
	global_load_lds_dwordx4 v[180:181], off
	s_mov_b32 m0, s1
	v_and_b32_e32 v191, 31, v0
	s_add_i32 s31, s30, 0x6000
	s_mov_b32 s1, m0
	s_mov_b32 m0, s31
	s_nop 0
	global_load_lds_dwordx4 v[182:183], off
	s_mov_b32 m0, s1
	s_mov_b64 s[14:15], 0x802000
	v_lshlrev_b32_e32 v195, 4, v192
	v_lshl_add_u64 v[2:3], v[48:49], 0, s[14:15]
	s_add_i32 s1, s30, 0x2000
	s_mov_b32 s14, m0
	s_mov_b32 m0, s1
	s_nop 0
	global_load_lds_dwordx4 v[2:3], off
	s_mov_b32 m0, s14
	v_lshl_or_b32 v1, v191, 7, v195
	global_load_dwordx4 v[136:139], v1, s[12:13]
	global_load_dwordx4 v[128:131], v1, s[12:13] offset:32
	global_load_dwordx4 v[120:123], v1, s[12:13] offset:64
	global_load_dwordx4 v[116:119], v1, s[12:13] offset:96
	s_mov_b64 s[14:15], 0x804000
	v_mov_b32_e32 v2, v185
	v_mov_b32_e32 v3, v185
	v_mov_b32_e32 v4, v185
	v_mov_b32_e32 v5, v185
	v_mov_b32_e32 v6, v185
	v_mov_b32_e32 v7, v185
	v_mov_b32_e32 v8, v185
	v_mov_b32_e32 v9, v185
	v_mov_b32_e32 v10, v185
	v_mov_b32_e32 v11, v185
	v_mov_b32_e32 v12, v185
	v_mov_b32_e32 v13, v185
	v_mov_b32_e32 v14, v185
	v_mov_b32_e32 v15, v185
	v_mov_b32_e32 v16, v185
	v_mov_b32_e32 v17, v185
	v_lshlrev_b32_e32 v1, 10, v192
	v_lshlrev_b32_e32 v18, 4, v191
	v_add3_u32 v198, 0, v1, v18
	v_lshl_add_u64 v[18:19], v[48:49], 0, s[14:15]
	s_add_i32 s1, s30, 0x4000
	s_mov_b32 s12, m0
	s_mov_b32 m0, s1
	s_nop 0
	global_load_lds_dwordx4 v[18:19], off
	s_mov_b32 m0, s12
	s_waitcnt vmcnt(3) lgkmcnt(0)
	s_barrier
	ds_read_b128 v[34:37], v198
	ds_read_b128 v[38:41], v198 offset:512
	v_lshlrev_b32_e32 v193, 3, v0
	s_mov_b64 s[16:17], 0x1002000
	s_add_i32 s1, s30, 0x8000
	s_lshl_b32 s0, s0, 2
	s_add_i32 s29, s0, 0
	s_add_u32 s2, s10, s2
	s_addc_u32 s3, s11, s3
	s_mov_b32 s20, -1
	s_movk_i32 s23, 0x2000
	s_movk_i32 s21, 0x4000
	s_mov_b64 s[10:11], 0x2000
	s_mov_b32 s22, 0x41000000
	s_mov_b64 s[14:15], 0x4000
	v_lshl_add_u32 v196, v191, 2, s29
	v_mov_b32_e32 v199, 0
	s_waitcnt vmcnt(3) lgkmcnt(1)
	v_mfma_f32_32x32x16_f16 v[18:33], v[34:37], v[136:139], v[2:17]
	s_waitcnt lgkmcnt(0)
	v_mfma_f32_32x32x16_f16 v[2:17], v[38:41], v[136:139], v[2:17]
	ds_read_b128 v[34:37], v198 offset:2048
	ds_read_b128 v[38:41], v198 offset:2560
	s_waitcnt vmcnt(2) lgkmcnt(1)
	v_mfma_f32_32x32x16_f16 v[18:33], v[34:37], v[128:131], v[18:33]
	s_waitcnt lgkmcnt(0)
	v_mfma_f32_32x32x16_f16 v[2:17], v[38:41], v[128:131], v[2:17]
	ds_read_b128 v[34:37], v198 offset:4096
	ds_read_b128 v[38:41], v198 offset:4608
	s_waitcnt vmcnt(1) lgkmcnt(1)
	v_mfma_f32_32x32x16_f16 v[18:33], v[34:37], v[120:123], v[18:33]
	s_waitcnt lgkmcnt(0)
	v_mfma_f32_32x32x16_f16 v[2:17], v[38:41], v[120:123], v[2:17]
	ds_read_b128 v[34:37], v198 offset:6144
	ds_read_b128 v[38:41], v198 offset:6656
	s_waitcnt vmcnt(0) lgkmcnt(1)
	v_mfma_f32_32x32x16_f16 v[18:33], v[34:37], v[116:119], v[18:33]
	s_waitcnt lgkmcnt(0)
	v_mfma_f32_32x32x16_f16 v[2:17], v[38:41], v[116:119], v[2:17]
	s_nop 9
	v_max_f32_e32 v1, v19, v19
	v_max_f32_e32 v34, v18, v18
	v_max_f32_e32 v1, v34, v1
	v_max3_f32 v35, v20, v21, v3
	v_max3_f32 v1, v1, v2, v4
	v_max3_f32 v34, v35, v24, v25
	v_max3_f32 v1, v1, v5, v22
	v_max3_f32 v34, v34, v8, v9
	v_max3_f32 v1, v1, v23, v6
	v_max3_f32 v34, v34, v28, v29
	v_max3_f32 v1, v1, v7, v26
	v_max3_f32 v34, v34, v12, v13
	v_max3_f32 v1, v1, v27, v10
	v_max3_f32 v34, v34, v32, v33
	v_max3_f32 v1, v1, v11, v30
	v_max3_f32 v34, v34, v16, v17
	v_max3_f32 v1, v1, v31, v14
	v_max3_f32 v1, v1, v15, v34
	v_mov_b32_e32 v34, v1
	s_nop 1
	v_permlane32_swap_b32_e32 v1, v34
	v_max_f32_e32 v34, v34, v34
	v_max_f32_e32 v1, v1, v1
	v_max_f32_e32 v197, v1, v34
	v_lshlrev_b32_e32 v1, 1, v0
	v_sub_f32_e32 v62, v32, v197
	v_and_b32_e32 v1, 32, v1
	v_and_b32_e32 v32, 24, v193
	v_lshlrev_b32_e32 v0, 4, v0
	v_add3_u32 v1, 0, v1, v32
	v_and_b32_e32 v0, 0xc0, v0
	v_lshlrev_b32_e32 v32, 8, v192
	v_add3_u32 v194, v1, v32, v0
	v_xor_b32_e32 v32, 0x80000000, v197
	v_sub_f32_e32 v63, v33, v197
	v_mov_b32_e32 v33, v32
	v_mov_b32_e32 v34, v32
	v_mov_b32_e32 v35, v32
	v_mov_b32_e32 v36, v32
	v_mov_b32_e32 v37, v32
	v_mov_b32_e32 v38, v32
	v_mov_b32_e32 v39, v32
	v_mov_b32_e32 v40, v32
	v_mov_b32_e32 v41, v32
	v_mov_b32_e32 v42, v32
	v_mov_b32_e32 v43, v32
	v_mov_b32_e32 v44, v32
	v_mov_b32_e32 v45, v32
	v_mov_b32_e32 v46, v32
	v_mov_b32_e32 v47, v32
	s_waitcnt vmcnt(0) lgkmcnt(0)
	s_barrier
	v_lshl_add_u64 v[0:1], v[48:49], 0, s[16:17]
	s_mov_b32 s12, m0
	s_mov_b32 m0, s1
	s_nop 0
	global_load_lds_dwordx4 v[0:1], off
	s_mov_b32 m0, s12
	s_mov_b64 s[12:13], 0x806000
	v_lshl_add_u64 v[0:1], v[48:49], 0, s[12:13]
	s_mov_b32 s1, m0
	s_mov_b32 m0, s30
	s_nop 0
	global_load_lds_dwordx4 v[0:1], off
	s_mov_b32 m0, s1
	ds_read_b128 v[172:175], v198 offset:8192
	ds_read_b128 v[168:171], v198 offset:8704
	ds_read_b128 v[164:167], v198 offset:10240
	ds_read_b128 v[160:163], v198 offset:10752
	ds_read_b128 v[156:159], v198 offset:12288
	ds_read_b128 v[152:155], v198 offset:12800
	ds_read_b128 v[148:151], v198 offset:14336
	ds_read_b128 v[144:147], v198 offset:14848
	v_sub_f32_e32 v18, v18, v197
	v_sub_f32_e32 v19, v19, v197
	v_sub_f32_e32 v20, v20, v197
	v_sub_f32_e32 v21, v21, v197
	v_sub_f32_e32 v22, v22, v197
	v_sub_f32_e32 v23, v23, v197
	v_sub_f32_e32 v24, v24, v197
	v_sub_f32_e32 v25, v25, v197
	v_sub_f32_e32 v26, v26, v197
	v_sub_f32_e32 v27, v27, v197
	v_sub_f32_e32 v28, v28, v197
	v_sub_f32_e32 v29, v29, v197
	v_sub_f32_e32 v30, v30, v197
	v_sub_f32_e32 v31, v31, v197
	v_sub_f32_e32 v2, v2, v197
	v_sub_f32_e32 v3, v3, v197
	v_sub_f32_e32 v4, v4, v197
	v_sub_f32_e32 v5, v5, v197
	v_sub_f32_e32 v6, v6, v197
	v_sub_f32_e32 v7, v7, v197
	v_sub_f32_e32 v8, v8, v197
	v_sub_f32_e32 v9, v9, v197
	v_sub_f32_e32 v10, v10, v197
	v_sub_f32_e32 v11, v11, v197
	v_sub_f32_e32 v12, v12, v197
	v_sub_f32_e32 v13, v13, v197
	v_sub_f32_e32 v14, v14, v197
	v_sub_f32_e32 v15, v15, v197
	v_sub_f32_e32 v16, v16, v197
	v_sub_f32_e32 v17, v17, v197
	v_exp_f32_e32 v64, v18
	v_exp_f32_e32 v65, v19
	v_exp_f32_e32 v48, v2
	v_exp_f32_e32 v49, v3
	v_exp_f32_e32 v66, v20
	v_exp_f32_e32 v50, v4
	v_mov_b32_e32 v67, v21
	v_mov_b32_e32 v51, v5
	v_exp_f32_e32 v68, v22
	v_exp_f32_e32 v52, v6
	v_exp_f32_e32 v69, v23
	v_exp_f32_e32 v53, v7
	v_exp_f32_e32 v70, v24
	v_exp_f32_e32 v54, v8
	v_mov_b32_e32 v71, v25
	v_mov_b32_e32 v55, v9
	v_exp_f32_e32 v72, v26
	v_exp_f32_e32 v56, v10
	v_exp_f32_e32 v73, v27
	v_exp_f32_e32 v57, v11
	v_exp_f32_e32 v74, v28
	v_exp_f32_e32 v58, v12
	v_mov_b32_e32 v75, v29
	v_mov_b32_e32 v59, v13
	v_exp_f32_e32 v76, v30
	v_exp_f32_e32 v60, v14
	v_exp_f32_e32 v77, v31
	v_exp_f32_e32 v61, v15
	v_exp_f32_e32 v78, v62
	v_exp_f32_e32 v62, v16
	v_mov_b32_e32 v79, v63
	v_mov_b32_e32 v63, v17
	s_waitcnt vmcnt(2) lgkmcnt(0)
	s_barrier
	v_or_b32_e32 v0, s2, v184
	v_mov_b32_e32 v1, s3
	v_lshl_add_u64 v[186:187], s[4:5], 0, v[0:1]
	s_mov_b32 s2, 0xff800000
	s_mov_b32 s4, 0xff806000
	v_cmp_gt_u32_e64 s[0:1], 32, v190
	s_mov_b32 s3, -1
	s_mov_b32 s5, -1
	s_mov_b64 s[12:13], 0x8000
	v_mov_b32_e32 v0, 0
	v_mov_b32_e32 v1, v185
	v_mov_b32_e32 v2, v185
	v_mov_b32_e32 v3, v185
	v_mov_b32_e32 v4, v185
	v_mov_b32_e32 v5, v185
	v_mov_b32_e32 v6, v185
	v_mov_b32_e32 v7, v185
	v_mov_b32_e32 v8, v185
	v_mov_b32_e32 v9, v185
	v_mov_b32_e32 v10, v185
	v_mov_b32_e32 v11, v185
	v_mov_b32_e32 v12, v185
	v_mov_b32_e32 v13, v185
	v_mov_b32_e32 v14, v185
	v_mov_b32_e32 v15, v185
	v_mov_b32_e32 v16, 0
	v_mov_b32_e32 v17, v185
	v_mov_b32_e32 v18, v185
	v_mov_b32_e32 v19, v185
	v_mov_b32_e32 v20, v185
	v_mov_b32_e32 v21, v185
	v_mov_b32_e32 v22, v185
	v_mov_b32_e32 v23, v185
	v_mov_b32_e32 v24, v185
	v_mov_b32_e32 v25, v185
	v_mov_b32_e32 v26, v185
	v_mov_b32_e32 v27, v185
	v_mov_b32_e32 v28, v185
	v_mov_b32_e32 v29, v185
	v_mov_b32_e32 v30, v185
	v_mov_b32_e32 v31, v185
	v_lshl_add_u64 v[188:189], v[186:187], 0, s[16:17]
	.p2align	6
